# trilive + early-out for chunks whose 4 key tiles are all masked-dead (skip QK tests, max, rescale, exp tests)
# baseline (speedup 1.0000x reference)
_Z7k_fusedPKDF16_S0_S0_S0_PKfS2_S2_Pf:
	v_lshrrev_b32_e32 v222, 6, v0
	v_and_b32_e32 v1, 63, v0
	s_load_dwordx8 s[24:31], s[0:1], 0x8
	s_load_dwordx4 s[36:39], s[0:1], 0x28
	v_lshlrev_b32_e32 v4, 2, v222
	v_lshlrev_b32_e32 v5, 3, v1
	v_lshl_or_b32 v2, v222, 11, v5
	v_lshlrev_b32_e32 v224, 12, v222
	v_or_b32_e32 v6, 1, v4
	v_lshlrev_b32_e32 v223, 1, v2
	v_readfirstlane_b32 s3, v224
	v_lshl_or_b32 v2, v6, 9, v5
	v_lshlrev_b32_e32 v225, 10, v6
	v_mov_b32_e32 v211, 0
	s_mov_b32 m0, s3
	v_lshlrev_b32_e32 v210, 1, v2
	v_readfirstlane_b32 s3, v225
	s_waitcnt lgkmcnt(0)
	global_load_lds_dwordx4 v223, s[24:25]
	v_lshl_add_u64 v[2:3], s[24:25], 0, v[210:211]
	s_mov_b32 m0, s3
	v_or_b32_e32 v6, 2, v4
	global_load_lds_dwordx4 v[2:3], off
	v_lshl_or_b32 v2, v6, 9, v5
	v_lshlrev_b32_e32 v212, 1, v2
	v_mov_b32_e32 v213, v211
	v_lshl_add_u64 v[2:3], s[24:25], 0, v[212:213]
	v_lshlrev_b32_e32 v213, 10, v6
	v_or_b32_e32 v4, 3, v4
	v_readfirstlane_b32 s3, v213
	s_mov_b32 m0, s3
	v_mov_b32_e32 v215, v211
	global_load_lds_dwordx4 v[2:3], off
	v_lshl_or_b32 v2, v4, 9, v5
	v_lshlrev_b32_e32 v214, 1, v2
	v_lshl_add_u64 v[2:3], s[24:25], 0, v[214:215]
	v_lshlrev_b32_e32 v215, 10, v4
	s_nop 0
	v_readfirstlane_b32 s3, v215
	s_mov_b32 m0, s3
	s_movk_i32 s3, 0xff
	global_load_lds_dwordx4 v[2:3], off
	v_and_b32_e32 v2, 0x7f, v0
	v_lshlrev_b32_e32 v2, 2, v2
	global_load_dword v4, v2, s[36:37]
	global_load_dword v5, v2, s[38:39]
	s_lshl_b32 s3, s2, 8
	s_load_dwordx2 s[4:5], s[0:1], 0x0
	v_and_b32_e32 v6, 0xff, v0
	v_or_b32_e32 v6, s3, v6
	v_ashrrev_i32_e32 v7, 31, v6
	v_lshl_add_u64 v[6:7], v[6:7], 2, s[30:31]
	global_load_dword v244, v[6:7], off
	v_mov_b32_e32 v208, s3
	v_lshl_or_b32 v2, s2, 3, v222
	v_ashrrev_i32_e32 v3, 31, v2
	v_lshlrev_b64 v[2:3], 13, v[2:3]
	s_waitcnt lgkmcnt(0)
	v_lshl_add_u64 v[6:7], s[4:5], 0, v[2:3]
	v_mov_b32_e32 v2, 0
	v_lshlrev_b32_e32 v206, 4, v1
	v_mov_b32_e32 v207, v2
	v_lshl_add_u64 v[6:7], v[6:7], 0, v[206:207]
	v_lshlrev_b32_e32 v211, 13, v222
	v_ashrrev_i32_e32 v209, 31, v208
	v_lshl_add_u64 v[8:9], v[208:209], 2, s[30:31]
	v_or_b32_e32 v3, v211, v206
	v_lshl_add_u64 v[8:9], v[8:9], 0, v[206:207]
	global_load_dwordx4 v[68:71], v[8:9], off
	global_load_dwordx4 v[130:133], v[6:7], off
	global_load_dwordx4 v[134:137], v[6:7], off offset:1024
	global_load_dwordx4 v[138:141], v[6:7], off offset:2048
	global_load_dwordx4 v[142:145], v[6:7], off offset:3072
	s_movk_i32 s33, 0x1000
	v_add_co_u32_e32 v14, vcc, s33, v6
	s_nop 1
	v_addc_co_u32_e32 v15, vcc, 0, v7, vcc
	global_load_dwordx4 v[146:149], v[14:15], off
	global_load_dwordx4 v[150:153], v[14:15], off offset:1024
	global_load_dwordx4 v[154:157], v[14:15], off offset:2048
	global_load_dwordx4 v[158:161], v[14:15], off offset:3072
	v_lshlrev_b32_e32 v10, 1, v3
	global_load_dwordx4 v[186:189], v10, s[28:29] offset:16
	global_load_dwordx4 v[190:193], v10, s[28:29]
	global_load_dwordx4 v[178:181], v10, s[28:29] offset:2064
	global_load_dwordx4 v[182:185], v10, s[28:29] offset:2048
	v_mov_b32_e32 v11, v2
	v_lshl_add_u64 v[8:9], s[28:29], 0, v[10:11]
	v_add_co_u32_e32 v12, vcc, s33, v8
	s_mov_b64 s[34:35], 0x1000
	s_nop 0
	v_addc_co_u32_e32 v13, vcc, 0, v9, vcc
	s_mov_b64 s[40:41], 0x1800
	v_lshl_add_u64 v[10:11], v[8:9], 0, s[34:35]
	v_lshl_add_u64 v[8:9], v[8:9], 0, s[40:41]
	global_load_dwordx4 v[170:173], v[12:13], off
	global_load_dwordx4 v[174:177], v[10:11], off offset:16
	global_load_dwordx4 v[162:165], v[12:13], off offset:2048
	global_load_dwordx4 v[166:169], v[8:9], off offset:16
	s_waitcnt vmcnt(17)
	v_cmp_gt_u32_e32 vcc, 0x100, v0
	s_and_saveexec_b64 s[4:5], vcc
	v_lshlrev_b32_e32 v12, 4, v0
	v_and_b32_e32 v13, 0xe3, v0
	v_lshlrev_b32_e32 v14, 1, v0
	v_and_b32_e32 v12, 64, v12
	s_mov_b32 s8, 0x20000
	v_and_b32_e32 v14, 48, v14
	v_lshl_or_b32 v13, v13, 2, v12
	v_or3_b32 v13, v13, v14, s8
	v_add_f32_e32 v12, -1.0, v244
	v_mul_f32_e32 v12, 0x47000000, v12
	v_mul_f32_e32 v12, 0x3fb8aa3b, v12
	ds_write_b32 v13, v12
	s_or_b64 exec, exec, s[4:5]
	s_waitcnt lgkmcnt(0)
	s_barrier
	ds_read_b128 v[4:7], v206 offset:8192
	ds_read_b128 v[72:75], v206 offset:9216
	s_load_dwordx2 s[30:31], s[0:1], 0x38
	s_mov_b32 s0, 0x47000000
	s_mov_b32 s42, 0x3fb8aa3b
	s_mov_b32 s43, 0xff800000
	v_lshrrev_b32_e32 v96, 5, v1
	v_lshlrev_b32_e32 v97, 4, v96
	v_lshl_or_b32 v209, v222, 11, v206
	v_lshlrev_b32_e32 v1, 5, v1
	s_add_u32 s54, s24, 0x8000
	v_lshlrev_b32_e32 v207, 2, v96
	s_addc_u32 s55, s25, 0
	v_or_b32_e32 v227, 0x10000, v3
	s_mov_b32 s56, 0xc1d00000
	s_mov_b64 s[44:45], 0x20000
	s_mov_b64 s[46:47], 0x20800
	s_mov_b64 s[48:49], 0x21000
	s_mov_b32 s57, 0x21000
	s_mov_b64 s[50:51], 0x21800
	v_mov_b32_e32 v194, 0x3c003c00
	s_waitcnt lgkmcnt(0)
	s_waitcnt vmcnt(15)
	v_mfma_f32_32x32x16_f16 v[36:51], v[4:7], v[130:133], 0
	ds_read_b128 v[4:7], v206
	ds_read_b128 v[76:79], v206 offset:1024
	ds_read_b128 v[20:23], v206 offset:24576
	ds_read_b128 v[80:83], v206 offset:25600
	ds_read_b128 v[52:55], v206 offset:16384
	ds_read_b128 v[84:87], v206 offset:17408
	v_max_f32_e32 v71, v71, v71
	s_waitcnt lgkmcnt(1)
	v_mfma_f32_32x32x16_f16 v[52:67], v[130:133], v[52:55], 0
	v_max_f32_e32 v70, v70, v70
	v_max_f32_e32 v70, v70, v71
	s_waitcnt vmcnt(14)
	v_mfma_f32_32x32x16_f16 v[36:51], v[72:75], v[134:137], v[36:51]
	s_waitcnt lgkmcnt(0)
	v_mfma_f32_32x32x16_f16 v[52:67], v[134:137], v[84:87], v[52:67]
	ds_read_b128 v[72:75], v206 offset:10240
	ds_read_b128 v[84:87], v206 offset:11264
	s_waitcnt lgkmcnt(1)
	s_waitcnt vmcnt(13)
	v_mfma_f32_32x32x16_f16 v[36:51], v[72:75], v[138:141], v[36:51]
	ds_read_b128 v[72:75], v206 offset:18432
	ds_read_b128 v[88:91], v206 offset:19456
	s_waitcnt lgkmcnt(1)
	v_mfma_f32_32x32x16_f16 v[52:67], v[138:141], v[72:75], v[52:67]
	ds_read_b128 v[72:75], v206 offset:12288
	s_waitcnt vmcnt(12)
	v_mfma_f32_32x32x16_f16 v[36:51], v[84:87], v[142:145], v[36:51]
	v_mbcnt_lo_u32_b32 v84, -1, 0
	v_mbcnt_hi_u32_b32 v92, -1, v84
	ds_read_b128 v[84:87], v206 offset:13312
	v_xor_b32_e32 v93, 1, v92
	v_xor_b32_e32 v94, 2, v92
	v_xor_b32_e32 v95, 4, v92
	s_waitcnt lgkmcnt(2)
	v_mfma_f32_32x32x16_f16 v[52:67], v[142:145], v[88:91], v[52:67]
	v_and_b32_e32 v88, 64, v92
	v_add_u32_e32 v98, 64, v88
	v_cmp_lt_i32_e32 vcc, v93, v98
	ds_read_b128 v[88:91], v206 offset:21504
	s_waitcnt lgkmcnt(2)
	s_waitcnt vmcnt(11)
	v_mfma_f32_32x32x16_f16 v[36:51], v[72:75], v[146:149], v[36:51]
	ds_read_b128 v[72:75], v206 offset:20480
	s_waitcnt lgkmcnt(0)
	v_mfma_f32_32x32x16_f16 v[52:67], v[146:149], v[72:75], v[52:67]
	v_cndmask_b32_e32 v72, v92, v93, vcc
	v_lshlrev_b32_e32 v72, 2, v72
	v_max3_f32 v73, v68, v69, v70
	ds_bpermute_b32 v72, v72, v73
	v_cmp_lt_i32_e32 vcc, v94, v98
	s_waitcnt lgkmcnt(0)
	v_max_f32_e32 v72, v72, v72
	v_cndmask_b32_e32 v68, v92, v94, vcc
	v_lshlrev_b32_e32 v74, 2, v68
	ds_read_b128 v[68:71], v206 offset:14336
	s_waitcnt vmcnt(10)
	v_mfma_f32_32x32x16_f16 v[36:51], v[84:87], v[150:153], v[36:51]
	v_max_f32_e32 v84, v73, v72
	ds_bpermute_b32 v85, v74, v84
	v_cmp_lt_i32_e32 vcc, v95, v98
	s_waitcnt lgkmcnt(0)
	v_max_f32_e32 v85, v85, v85
	v_mfma_f32_32x32x16_f16 v[52:67], v[150:153], v[88:91], v[52:67]
	v_cndmask_b32_e32 v72, v92, v95, vcc
	v_lshlrev_b32_e32 v86, 2, v72
	v_max_f32_e32 v92, v84, v85
	ds_read_b128 v[72:75], v206 offset:15360
	ds_bpermute_b32 v93, v86, v92
	s_waitcnt lgkmcnt(0)
	v_max_f32_e32 v93, v93, v93
	s_waitcnt vmcnt(9)
	v_mfma_f32_32x32x16_f16 v[36:51], v[68:71], v[154:157], v[36:51]
	ds_read_b128 v[68:71], v206 offset:22528
	ds_read_b128 v[84:87], v206 offset:23552
	v_max_f32_e32 v92, v92, v93
	global_load_dwordx4 v[88:91], v97, s[36:37]
	v_readlane_b32 s3, v92, 0
	v_readlane_b32 s2, v92, 8
	v_readlane_b32 s5, v92, 16
	v_readlane_b32 s4, v92, 24
	s_waitcnt lgkmcnt(1)
	v_mfma_f32_32x32x16_f16 v[52:67], v[154:157], v[68:71], v[52:67]
	v_add_f32_e64 v68, s2, -1.0
	v_add_f32_e64 v69, s3, -1.0
	v_readlane_b32 s7, v92, 32
	v_readlane_b32 s6, v92, 40
	v_add_f32_e64 v70, s4, -1.0
	v_add_f32_e64 v71, s5, -1.0
	v_pk_mul_f32 v[68:69], v[68:69], s[0:1] op_sel_hi:[1,0]
	v_readlane_b32 s9, v92, 48
	v_readlane_b32 s8, v92, 56
	v_mfma_f32_32x32x16_f16 v[20:35], v[20:23], v[130:133], 0
	v_mul_f32_e64 v70, v70, s0
	v_mul_f32_e64 v71, v71, s0
	v_mul_f32_e64 v92, v68, s42
	v_mul_f32_e64 v93, v69, s42
	v_mul_f32_e64 v94, v70, s42
	v_mul_f32_e64 v95, v71, s42
	v_max3_f32 v68, v93, s43, v92
	v_max3_f32 v68, v68, v95, v94
	s_waitcnt vmcnt(9)
	v_mfma_f32_32x32x16_f16 v[36:51], v[72:75], v[158:161], v[36:51]
	v_add_f32_e64 v72, s6, -1.0
	v_add_f32_e64 v73, s7, -1.0
	v_mul_f32_e64 v72, v72, s0
	v_mul_f32_e64 v73, v73, s0
	s_waitcnt lgkmcnt(0)
	v_mfma_f32_32x32x16_f16 v[52:67], v[158:161], v[84:87], v[52:67]
	v_mul_f32_e64 v84, v72, s42
	v_mul_f32_e64 v85, v73, s42
	v_add_f32_e64 v86, s8, -1.0
	v_add_f32_e64 v87, s9, -1.0
	v_max3_f32 v98, v68, v85, v84
	ds_read_b128 v[68:71], v206 offset:26624
	v_cvt_pk_f16_f32 v43, v42, v43
	v_cvt_pk_f16_f32 v42, v40, v41
	v_cvt_pk_f16_f32 v41, v38, v39
	v_mfma_f32_32x32x16_f16 v[20:35], v[80:83], v[134:137], v[20:35]
	v_mul_f32_e64 v80, v86, s0
	v_mul_f32_e64 v81, v87, s0
	v_cvt_pk_f16_f32 v40, v36, v37
	v_mul_f32_e64 v86, v80, s42
	v_mul_f32_e64 v87, v81, s42
	global_load_dwordx4 v[72:75], v97, s[36:37] offset:32
	v_max3_f32 v80, v98, v87, v86
	v_add_f32_e32 v98, 0xc53b8000, v80
	ds_read_b128 v[80:83], v206 offset:27648
	global_load_dwordx4 v[36:39], v97, s[36:37] offset:64
	ds_write_b128 v209, v[40:43] offset:32768
	v_cvt_pk_f16_f32 v43, v50, v51
	v_cvt_pk_f16_f32 v40, v44, v45
	v_cvt_pk_f16_f32 v44, v52, v53
	global_load_dwordx4 v[50:53], v97, s[36:37] offset:96
	s_waitcnt lgkmcnt(2)
	v_mfma_f32_32x32x16_f16 v[20:35], v[68:71], v[138:141], v[20:35]
	ds_read_b128 v[68:71], v206 offset:28672
	v_cvt_pk_f16_f32 v42, v48, v49
	v_cvt_pk_f16_f32 v41, v46, v47
	ds_write_b128 v209, v[40:43] offset:33792
	ds_read_b128 v[40:43], v206 offset:30720
	v_cvt_pk_f16_f32 v47, v58, v59
	v_cvt_pk_f16_f32 v46, v56, v57
	s_waitcnt lgkmcnt(4)
	v_mfma_f32_32x32x16_f16 v[20:35], v[80:83], v[142:145], v[20:35]
	ds_read_b128 v[80:83], v206 offset:29696
	v_cvt_pk_f16_f32 v45, v54, v55
	ds_write_b128 v209, v[44:47] offset:49152
	v_cvt_pk_f16_f32 v45, v66, v67
	ds_read_b128 v[46:49], v206 offset:31744
	v_cvt_pk_f16_f32 v44, v64, v65
	v_cmp_ge_f32_e64 s[0:1], v92, v98
	s_waitcnt lgkmcnt(5)
	v_mfma_f32_32x32x16_f16 v[20:35], v[68:71], v[146:149], v[20:35]
	v_cmp_ge_f32_e64 s[2:3], v93, v98
	v_cmp_ge_f32_e64 s[4:5], v94, v98
	v_cmp_ge_f32_e64 s[6:7], v95, v98
	v_cmp_ge_f32_e64 s[8:9], v84, v98
	v_cmp_ge_f32_e64 s[10:11], v85, v98
	v_cmp_ge_f32_e64 s[12:13], v86, v98
	v_cmp_ge_f32_e64 s[14:15], v87, v98
	v_mfma_f32_32x32x16_f16 v[4:19], v[4:7], v[130:133], 0
	s_waitcnt lgkmcnt(2)
	v_mfma_f32_32x32x16_f16 v[20:35], v[80:83], v[150:153], v[20:35]
	v_mfma_f32_32x32x16_f16 v[4:19], v[76:79], v[134:137], v[4:19]
	v_mfma_f32_32x32x16_f16 v[20:35], v[40:43], v[154:157], v[20:35]
	v_cvt_pk_f16_f32 v43, v62, v63
	v_cvt_pk_f16_f32 v42, v60, v61
	ds_write_b128 v209, v[42:45] offset:50176
	ds_read_b128 v[40:43], v206 offset:2048
	ds_read_b128 v[54:57], v206 offset:3072
	s_waitcnt lgkmcnt(1)
	v_mfma_f32_32x32x16_f16 v[4:19], v[40:43], v[138:141], v[4:19]
	s_waitcnt lgkmcnt(0)
	v_mfma_f32_32x32x16_f16 v[4:19], v[54:57], v[142:145], v[4:19]
	v_mfma_f32_32x32x16_f16 v[20:35], v[46:49], v[158:161], v[20:35]
	ds_read_b128 v[44:47], v206 offset:4096
	ds_read_b128 v[58:61], v206 offset:5120
	ds_read_b128 v[62:65], v206 offset:6144
	ds_read_b128 v[66:69], v206 offset:7168
	s_waitcnt lgkmcnt(0)
	s_barrier
	s_waitcnt vmcnt(3)
	s_nop 4
	v_add_f32_e32 v20, v20, v88
	v_mfma_f32_32x32x16_f16 v[4:19], v[44:47], v[146:149], v[4:19]
	v_add_f32_e32 v21, v89, v21
	v_add_f32_e32 v22, v90, v22
	v_add_f32_e32 v23, v91, v23
	s_waitcnt vmcnt(2)
	v_add_f32_e32 v24, v24, v72
	v_add_f32_e32 v25, v73, v25
	v_add_f32_e32 v26, v74, v26
	v_add_f32_e32 v27, v75, v27
	v_mfma_f32_32x32x16_f16 v[4:19], v[58:61], v[150:153], v[4:19]
	s_waitcnt vmcnt(1)
	v_add_f32_e32 v28, v28, v36
	v_add_f32_e32 v29, v37, v29
	v_add_f32_e32 v30, v38, v30
	v_add_f32_e32 v31, v39, v31
	s_waitcnt vmcnt(0)
	v_add_f32_e32 v32, v32, v50
	v_add_f32_e32 v33, v51, v33
	v_add_f32_e32 v34, v52, v34
	v_mfma_f32_32x32x16_f16 v[4:19], v[62:65], v[154:157], v[4:19]
	v_add_f32_e32 v35, v53, v35
	v_mul_f32_e32 v20, 0xbfb8aa3b, v20
	v_mul_f32_e32 v21, 0xbfb8aa3b, v21
	v_mul_f32_e32 v22, 0xbfb8aa3b, v22
	v_mul_f32_e32 v23, 0xbfb8aa3b, v23
	v_mul_f32_e32 v24, 0xbfb8aa3b, v24
	v_mul_f32_e32 v25, 0xbfb8aa3b, v25
	v_mfma_f32_32x32x16_f16 v[4:19], v[66:69], v[158:161], v[4:19]
	v_mul_f32_e32 v26, 0xbfb8aa3b, v26
	v_mul_f32_e32 v27, 0xbfb8aa3b, v27
	v_mul_f32_e32 v28, 0xbfb8aa3b, v28
	v_mul_f32_e32 v29, 0xbfb8aa3b, v29
	v_mul_f32_e32 v30, 0xbfb8aa3b, v30
	v_mul_f32_e32 v31, 0xbfb8aa3b, v31
	v_mul_f32_e32 v32, 0xbfb8aa3b, v32
	v_mul_f32_e32 v33, 0xbfb8aa3b, v33
	v_mul_f32_e32 v34, 0xbfb8aa3b, v34
	v_mul_f32_e32 v35, 0xbfb8aa3b, v35
	v_exp_f32_e32 v20, v20
	v_exp_f32_e32 v21, v21
	v_exp_f32_e32 v22, v22
	v_exp_f32_e32 v23, v23
	v_exp_f32_e32 v24, v24
	v_exp_f32_e32 v25, v25
	v_exp_f32_e32 v26, v26
	v_exp_f32_e32 v27, v27
	v_exp_f32_e32 v28, v28
	v_exp_f32_e32 v29, v29
	v_exp_f32_e32 v30, v30
	v_exp_f32_e32 v31, v31
	v_exp_f32_e32 v32, v32
	v_exp_f32_e32 v33, v33
	v_exp_f32_e32 v34, v34
	v_exp_f32_e32 v35, v35
	v_add_f32_e32 v20, 1.0, v20
	v_add_f32_e32 v21, 1.0, v21
	v_add_f32_e32 v22, 1.0, v22
	v_add_f32_e32 v23, 1.0, v23
	v_add_f32_e32 v24, 1.0, v24
	v_add_f32_e32 v25, 1.0, v25
	v_add_f32_e32 v26, 1.0, v26
	v_add_f32_e32 v27, 1.0, v27
	v_add_f32_e32 v28, 1.0, v28
	v_add_f32_e32 v29, 1.0, v29
	v_add_f32_e32 v30, 1.0, v30
	v_add_f32_e32 v31, 1.0, v31
	v_add_f32_e32 v32, 1.0, v32
	v_add_f32_e32 v33, 1.0, v33
	v_add_f32_e32 v34, 1.0, v34
	v_add_f32_e32 v35, 1.0, v35
	v_rcp_f32_e32 v20, v20
	v_rcp_f32_e32 v21, v21
	v_rcp_f32_e32 v22, v22
	v_rcp_f32_e32 v23, v23
	v_rcp_f32_e32 v24, v24
	v_rcp_f32_e32 v25, v25
	v_rcp_f32_e32 v26, v26
	v_rcp_f32_e32 v27, v27
	v_rcp_f32_e32 v28, v28
	v_rcp_f32_e32 v29, v29
	v_rcp_f32_e32 v30, v30
	v_rcp_f32_e32 v31, v31
	v_rcp_f32_e32 v32, v32
	v_rcp_f32_e32 v33, v33
	v_rcp_f32_e32 v34, v34
	v_rcp_f32_e32 v35, v35
	v_cvt_pk_f16_f32 v198, v4, v5
	v_lshl_or_b32 v4, v222, 14, v1
	v_mov_b32_e32 v5, v2
	v_lshl_add_u64 v[216:217], s[28:29], 0, v[4:5]
	v_or_b32_e32 v4, 0x2000, v4
	v_lshrrev_b32_e32 v1, 1, v0
	v_lshl_add_u64 v[218:219], s[28:29], 0, v[4:5]
	v_and_b32_e32 v4, 16, v1
	v_mov_b32_e32 v36, 0x20000
	v_lshl_add_u64 v[4:5], s[36:37], 0, v[4:5]
	s_mov_b64 s[28:29], 0x80
	v_lshl_or_b32 v226, v96, 6, v36
	v_cvt_pk_f16_f32 v199, v6, v7
	v_cvt_pk_f16_f32 v200, v8, v9
	v_cvt_pk_f16_f32 v201, v10, v11
	v_cvt_pk_f16_f32 v202, v12, v13
	v_cvt_pk_f16_f32 v203, v14, v15
	v_cvt_pk_f16_f32 v204, v16, v17
	v_cvt_pk_f16_f32 v205, v18, v19
	v_cvt_pk_f16_f32 v229, v20, v21
	v_cvt_pk_f16_f32 v230, v22, v23
	v_cvt_pk_f16_f32 v232, v24, v25
	v_cvt_pk_f16_f32 v234, v26, v27
	v_cvt_pk_f16_f32 v228, v28, v29
	v_cvt_pk_f16_f32 v231, v30, v31
	v_cvt_pk_f16_f32 v233, v32, v33
	v_cvt_pk_f16_f32 v235, v34, v35
	v_lshl_add_u64 v[220:221], v[4:5], 0, s[28:29]
	s_mov_b64 s[36:37], 0
	s_or_b64 s[74:75], s[0:1], s[2:3]
	s_or_b64 s[76:77], s[4:5], s[6:7]
	s_or_b64 s[74:75], s[74:75], s[76:77]
	s_cmp_eq_u64 s[74:75], 0
	s_cselect_b32 s72, 1, 0
	s_or_b64 s[74:75], s[8:9], s[10:11]
	s_or_b64 s[76:77], s[12:13], s[14:15]
	s_or_b64 s[74:75], s[74:75], s[76:77]
	s_cmp_eq_u64 s[74:75], 0
	s_cselect_b32 s73, 1, 0
	s_branch .LBB1_6

.LBB1_6:
	v_mov_b32_e32 v195, v194
	v_mov_b32_e32 v196, v194
	v_mov_b32_e32 v197, v194
	s_setprio 1
	s_cmp_lg_u32 s72, 0
	s_cbranch_scc1 .LBB1_11
	s_and_b64 vcc, exec, s[2:3]
	s_cbranch_vccnz .LBB1_61
	v_cndmask_b32_e64 v1, 0, 1, s[0:1]
	v_cmp_ne_u32_e64 s[16:17], 1, v1
	s_andn2_b64 vcc, exec, s[0:1]
	s_cbranch_vccz .LBB1_62

.Ltri1_done:
	s_cmp_lg_u32 s36, 0x60000
	s_cselect_b64 s[52:53], -1, 0
	s_cmp_eq_u32 s36, 0x60000
	s_cselect_b32 s23, s27, s55
	s_cselect_b32 s22, s26, s54
	s_setprio 0
	v_readfirstlane_b32 s24, v224
	s_mov_b32 m0, s24
	v_readfirstlane_b32 s24, v225
	global_load_lds_dwordx4 v223, s[22:23]
	s_mov_b32 m0, s24
	v_readfirstlane_b32 s24, v213
	global_load_lds_dwordx4 v210, s[22:23]
	s_mov_b32 m0, s24
	v_readfirstlane_b32 s24, v215
	global_load_lds_dwordx4 v212, s[22:23]
	s_mov_b32 m0, s24
	v_cndmask_b32_e64 v1, 0, 1, s[2:3]
	global_load_lds_dwordx4 v214, s[22:23]
	s_cmp_lg_u32 s72, 0
	s_cbranch_scc1 .Lc0_dead_tail
	v_mov_b32_e32 v243, 0xff800000
	v_cmp_ne_u32_e64 s[22:23], 1, v1
	s_andn2_b64 vcc, exec, s[2:3]
	v_mov_b32_e32 v1, 0xff800000
	s_cbranch_vccz .LBB1_64
	s_and_b64 vcc, exec, s[22:23]
	s_cbranch_vccz .LBB1_65

.LBB1_32:
	s_setprio 0
	s_setprio 1
	s_cmp_lg_u32 s73, 0
	s_cbranch_scc1 .LBB1_36
	v_cndmask_b32_e64 v1, 0, 1, s[10:11]
	v_cmp_ne_u32_e64 s[18:19], 1, v1
	s_andn2_b64 vcc, exec, s[10:11]
	s_cbranch_vccz .LBB1_71
	v_cndmask_b32_e64 v1, 0, 1, s[8:9]
	v_cmp_ne_u32_e64 s[20:21], 1, v1
	s_andn2_b64 vcc, exec, s[8:9]
	s_cbranch_vccz .LBB1_72

.LBB1_38:
	s_cmp_lg_u32 s73, 0
	s_cbranch_scc1 .LBB1_59
	s_setprio 0
	v_mov_b32_e32 v16, 0xff800000
	s_and_b64 vcc, exec, s[18:19]
	v_mov_b32_e32 v1, 0xff800000
	s_cbranch_vccz .LBB1_75
	s_and_b64 vcc, exec, s[18:19]
	s_cbranch_vccz .LBB1_76

.Lc0_dead_tail:
	v_mov_b32_e32 v236, 0xff800000
	v_mov_b64_e32 v[82:83], 0
	v_mov_b64_e32 v[84:85], 0
	v_mov_b64_e32 v[86:87], 0
	v_mov_b64_e32 v[88:89], 0
	v_mov_b64_e32 v[90:91], 0
	v_mov_b64_e32 v[92:93], 0
	v_mov_b64_e32 v[94:95], 0
	v_mov_b64_e32 v[96:97], 0
	v_mov_b64_e32 v[98:99], 0
	v_mov_b64_e32 v[100:101], 0
	v_mov_b64_e32 v[102:103], 0
	v_mov_b64_e32 v[104:105], 0
	v_mov_b64_e32 v[106:107], 0
	v_mov_b64_e32 v[108:109], 0
	v_mov_b64_e32 v[110:111], 0
	v_mov_b64_e32 v[112:113], 0
	s_branch .LBB1_32
